# kernel start: the two XCD-placement compare-and-swap results are consumed just before the first grid barrier instead of being waited for before the prologue work
# baseline (speedup 1.0000x reference)
; __device__ __forceinline__ unsigned xb_add(unsigned* p, unsigned v) { return __hip_atomic_fetch_add(p, v, __ATOMIC_RELAXED, __HIP_MEMORY_SCOPE_AGENT); }
; __global__ void __launch_bounds__(NWAVES * 64, 2) mega(Args args) {
;     ...
;     if (MK_LOCALBAR && F.tid == 0) {
;         unsigned* rec = (unsigned*)(F.ctl + CW_LBAR + (25 + ((int)blockIdx.x & 7)) * 64); const unsigned mine = (bar.x & 15u) + 1u; unsigned expect = 0u;
;         if (!__hip_atomic_compare_exchange_strong(rec, &expect, mine, __ATOMIC_RELAXED, __ATOMIC_RELAXED, __HIP_MEMORY_SCOPE_AGENT) && expect != mine) (void)xb_add((unsigned*)(F.ctl + CW_LBAR + 24 * 64), 1u);
;         unsigned* rec2 = (unsigned*)(F.ctl + CW_LBAR + (33 + (int)(bar.x & 15u)) * 64); const unsigned grp = ((unsigned)blockIdx.x & 7u) + 1u; expect = 0u;
;         if (!__hip_atomic_compare_exchange_strong(rec2, &expect, grp, __ATOMIC_RELAXED, __ATOMIC_RELAXED, __HIP_MEMORY_SCOPE_AGENT) && expect != grp) (void)xb_add((unsigned*)(F.ctl + CW_LBAR + 24 * 64), 1u);
;     }
.LBB0_10:
	s_lshl_b32 s4, s2, 8
	s_and_b32 s4, s4, 0x700
	s_add_u32 s4, s30, s4
	s_addc_u32 s5, s31, 0
	s_add_i32 s8, s33, 1
	v_mov_b32_e32 v2, s8
	v_mov_b32_e32 v3, 0
	v_mov_b32_e32 v250, 0x31000
	global_atomic_cmpswap v250, v250, v[2:3], s[4:5] offset:2304 sc0
	s_lshl_b32 s4, s33, 8
	s_add_u32 s4, s30, s4
	s_addc_u32 s5, s31, 0
	s_and_b32 s8, s2, 7
	s_add_i32 s8, s8, 1
	v_mov_b32_e32 v4, s8
	v_mov_b32_e32 v5, 0
	v_mov_b32_e32 v251, 0x32000
	global_atomic_cmpswap v251, v251, v[4:5], s[4:5] offset:256 sc0

; __device__ __forceinline__ int mk_lane() { int l_ = (int)__builtin_amdgcn_mbcnt_hi(~0u, __builtin_amdgcn_mbcnt_lo(~0u, 0u)); asm volatile("" : "+v"(l_)); return l_; }
; __device__ __forceinline__ unsigned xb_add(unsigned* p, unsigned v) { return __hip_atomic_fetch_add(p, v, __ATOMIC_RELAXED, __HIP_MEMORY_SCOPE_AGENT); }
; __device__ __forceinline__ void xcd_barrier(const XcdBarrier& b, int wave_id, int pair = -1) {
;     asm volatile("s_waitcnt vmcnt(0)" ::: "memory");
;     __syncthreads();
;     if (wave_id == 0 && mk_lane() == 0) {
;         unsigned* bar = b.bar;
;         __builtin_amdgcn_s_waitcnt(0);
;         unsigned nloc = b.st[0], nx = b.st[1];
;         if (nloc == 0u) { xcd_barrier_complete(bar, b.x, nloc, nx); b.st[0] = nloc; b.st[1] = nx; }
; __global__ void __launch_bounds__(NWAVES * 64, 2) mega(Args args) {
;     ...
;     if (MK_LOCALBAR && F.tid == 0) {
;         unsigned* rec = (unsigned*)(F.ctl + CW_LBAR + (25 + ((int)blockIdx.x & 7)) * 64); const unsigned mine = (bar.x & 15u) + 1u; unsigned expect = 0u;
;         if (!__hip_atomic_compare_exchange_strong(rec, &expect, mine, __ATOMIC_RELAXED, __ATOMIC_RELAXED, __HIP_MEMORY_SCOPE_AGENT) && expect != mine) (void)xb_add((unsigned*)(F.ctl + CW_LBAR + 24 * 64), 1u);
;         unsigned* rec2 = (unsigned*)(F.ctl + CW_LBAR + (33 + (int)(bar.x & 15u)) * 64); const unsigned grp = ((unsigned)blockIdx.x & 7u) + 1u; expect = 0u;
;         if (!__hip_atomic_compare_exchange_strong(rec2, &expect, grp, __ATOMIC_RELAXED, __ATOMIC_RELAXED, __HIP_MEMORY_SCOPE_AGENT) && expect != grp) (void)xb_add((unsigned*)(F.ctl + CW_LBAR + 24 * 64), 1u);
.LBB0_54:
	s_or_b64 exec, exec, s[12:13]
	s_cmp_gt_i32 s41, 1
	s_cbranch_scc0 .LBB0_110
	s_cmp_lg_u32 s61, 0
	s_cbranch_scc1 .Lrec_skip
	s_mov_b64 s[98:99], exec
	s_mov_b64 exec, 1
	s_waitcnt vmcnt(0)
	s_add_i32 s4, s33, 1
	v_cmp_ne_u32_e32 vcc, 0, v250
	v_cmp_ne_u32_e64 s[6:7], s4, v250
	s_and_b64 s[6:7], vcc, s[6:7]
	s_and_b32 s5, s2, 7
	s_add_i32 s5, s5, 1
	v_cmp_ne_u32_e32 vcc, 0, v251
	v_cmp_ne_u32_e64 s[8:9], s5, v251
	s_and_b64 s[8:9], vcc, s[8:9]
	s_and_b32 s6, s6, 1
	s_and_b32 s8, s8, 1
	s_add_i32 s6, s6, s8
	s_cmp_eq_u32 s6, 0
	s_cbranch_scc1 .Lrec_none
	v_mov_b32_e32 v250, 0x31000
	v_mov_b32_e32 v251, s6
	global_atomic_add v250, v251, s[30:31] offset:2048
.Lrec_none:
	s_mov_b64 exec, s[98:99]
.Lrec_skip:
	s_waitcnt vmcnt(0)
	s_andn2_b64 vcc, exec, s[38:39]
	s_barrier
	s_cbranch_vccnz .LBB0_109
	v_mbcnt_lo_u32_b32 v0, -1, 0
	v_mbcnt_hi_u32_b32 v0, -1, v0
	s_nop 0
	v_cmp_eq_u32_e32 vcc, 0, v0
	s_and_saveexec_b64 s[4:5], vcc
	s_cbranch_execz .LBB0_108
	s_add_i32 s3, 0, 0x27f60
	v_mov_b32_e32 v0, s3
	s_waitcnt vmcnt(0) expcnt(0) lgkmcnt(0)
	ds_read_b32 v2, v0
	s_add_i32 s3, 0, 0x27f64
	v_mov_b32_e32 v0, s3
	ds_read_b32 v0, v0
	s_waitcnt lgkmcnt(1)
	v_cmp_ne_u32_e32 vcc, 0, v2
	s_cbranch_vccnz .LBB0_72
	v_readlane_b32 s6, v248, 0
	v_readlane_b32 s7, v248, 1
	s_load_dwordx2 s[10:11], s[6:7], 0x4
	s_add_u32 s6, s30, 0x4200
	s_addc_u32 s7, s31, 0
	s_add_u32 s8, s30, 0x4400
	s_addc_u32 s9, s31, 0
	s_waitcnt lgkmcnt(0)
	s_mul_i32 s3, s10, s60
	s_add_u32 s10, s30, 0x4500
	s_mul_i32 s3, s3, s11
	s_addc_u32 s11, s31, 0
	s_add_u32 s12, s30, 0x4600
	s_addc_u32 s13, s31, 0
	s_add_u32 s14, s30, 0x4700
	s_addc_u32 s15, s31, 0
	s_add_u32 s16, s30, 0x4800
	s_addc_u32 s17, s31, 0
	s_add_u32 s18, s30, 0x4900
	s_addc_u32 s19, s31, 0
	s_add_u32 s20, s30, 0x4a00
	s_addc_u32 s21, s31, 0
	s_add_u32 s22, s30, 0x4b00
	s_addc_u32 s23, s31, 0
	s_add_u32 s24, s30, 0x4c00
	s_addc_u32 s25, s31, 0
	s_add_u32 s26, s30, 0x4d00
	s_addc_u32 s27, s31, 0
	s_add_u32 s28, s30, 0x4e00
	s_addc_u32 s29, s31, 0
	s_add_u32 s42, s30, 0x4f00
	s_addc_u32 s43, s31, 0
	s_add_u32 s44, s30, 0x5000
	s_addc_u32 s45, s31, 0
	s_add_u32 s46, s30, 0x5100
	s_addc_u32 s47, s31, 0
	s_add_u32 s48, s30, 0x5200
	s_addc_u32 s49, s31, 0
	s_add_u32 s50, s30, 0x5300
	s_addc_u32 s51, s31, 0
	s_mov_b32 s58, 1
	v_mov_b32_e32 v16, 0
	s_branch .LBB0_60

; __global__ void __launch_bounds__(NWAVES * 64, 2) mega(Args args) {
	.amdhsa_kernel _Z4mega4Args
		.amdhsa_group_segment_fixed_size 0
		.amdhsa_private_segment_fixed_size 0
		.amdhsa_kernarg_size 400
		.amdhsa_user_sgpr_count 2
		.amdhsa_user_sgpr_dispatch_ptr 0
		.amdhsa_user_sgpr_queue_ptr 0
		.amdhsa_user_sgpr_kernarg_segment_ptr 1
		.amdhsa_user_sgpr_dispatch_id 0
		.amdhsa_user_sgpr_kernarg_preload_length 0
		.amdhsa_user_sgpr_kernarg_preload_offset 0
		.amdhsa_user_sgpr_private_segment_size 0
		.amdhsa_uses_dynamic_stack 0
		.amdhsa_enable_private_segment 0
		.amdhsa_system_sgpr_workgroup_id_x 1
		.amdhsa_system_sgpr_workgroup_id_y 0
		.amdhsa_system_sgpr_workgroup_id_z 0
		.amdhsa_system_sgpr_workgroup_info 0
		.amdhsa_system_vgpr_workitem_id 0
		.amdhsa_next_free_vgpr 256
		.amdhsa_next_free_sgpr 102
		.amdhsa_accum_offset 256
		.amdhsa_reserve_vcc 1
		.amdhsa_float_round_mode_32 0
		.amdhsa_float_round_mode_16_64 0
		.amdhsa_float_denorm_mode_32 3
		.amdhsa_float_denorm_mode_16_64 3
		.amdhsa_dx10_clamp 1
		.amdhsa_ieee_mode 1
		.amdhsa_fp16_overflow 0
		.amdhsa_tg_split 0
		.amdhsa_exception_fp_ieee_invalid_op 0
		.amdhsa_exception_fp_denorm_src 0
		.amdhsa_exception_fp_ieee_div_zero 0
		.amdhsa_exception_fp_ieee_overflow 0
		.amdhsa_exception_fp_ieee_underflow 0
		.amdhsa_exception_fp_ieee_inexact 0
		.amdhsa_exception_int_div_zero 0
	.end_amdhsa_kernel

; __global__ void __launch_bounds__(NWAVES * 64, 2) mega(Args args) {
amdhsa.kernels:
  - .agpr_count:     0
    .args:
      - .offset:         0
        .size:           144
        .value_kind:     by_value
      - .offset:         144
        .size:           4
        .value_kind:     hidden_block_count_x
      - .offset:         148
        .size:           4
        .value_kind:     hidden_block_count_y
      - .offset:         152
        .size:           4
        .value_kind:     hidden_block_count_z
      - .offset:         156
        .size:           2
        .value_kind:     hidden_group_size_x
      - .offset:         158
        .size:           2
        .value_kind:     hidden_group_size_y
      - .offset:         160
        .size:           2
        .value_kind:     hidden_group_size_z
      - .offset:         162
        .size:           2
        .value_kind:     hidden_remainder_x
      - .offset:         164
        .size:           2
        .value_kind:     hidden_remainder_y
      - .offset:         166
        .size:           2
        .value_kind:     hidden_remainder_z
      - .offset:         184
        .size:           8
        .value_kind:     hidden_global_offset_x
      - .offset:         192
        .size:           8
        .value_kind:     hidden_global_offset_y
      - .offset:         200
        .size:           8
        .value_kind:     hidden_global_offset_z
      - .offset:         208
        .size:           2
        .value_kind:     hidden_grid_dims
      - .offset:         264
        .size:           4
        .value_kind:     hidden_dynamic_lds_size
    .group_segment_fixed_size: 0
    .kernarg_segment_align: 8
    .kernarg_segment_size: 400
    .language:       OpenCL C
    .language_version:
      - 2
      - 0
    .max_flat_workgroup_size: 512
    .name:           _Z4mega4Args
    .private_segment_fixed_size: 0
    .sgpr_count:     108
    .sgpr_spill_count: 4
    .symbol:         _Z4mega4Args.kd
    .uniform_work_group_size: 1
    .uses_dynamic_stack: false
    .vgpr_count:     256
    .vgpr_spill_count: 0
    .wavefront_size: 64
